# attention tile body rewritten: batched QK reads, max3 tree, permlane swap, plain v_exp on p-max, packed sums
# baseline (speedup 1.0000x reference)
; DI int crow(int r, int hi) { return (r & 3) + 8 * (r >> 2) + 4 * hi; }
; #define MFMA32(a, b, c) __builtin_amdgcn_mfma_f32_32x32x16_bf16((a), (b), (c), 0, 0, 0)
; DI s16x4 tr16(const LAS char* p) { typedef short v4i16_t __attribute__((ext_vector_type(4))); return __builtin_bit_cast(s16x4, __builtin_amdgcn_ds_read_tr16_b64_v4i16((LAS v4i16_t*)p)); }
; DI bf16x8 cat8(s16x4 lo, s16x4 hi) { return __builtin_shufflevector(lo, hi, 0, 1, 2, 3, 4, 5, 6, 7); }
; DI void attn_unit(const Params& p, int bh, int qb, char* lds, volatile LAS unsigned* hbc, unsigned& hbph) {
;     ...
;     f32x16 p0, p1;
; #pragma unroll
;     for (int g = 0; g < 4; ++g) { const f32x4 a = *(const f32x4*)(Fs + 8 * g + 4 * hi), c = *(const f32x4*)(Fs + 32 + 8 * g + 4 * hi);
; #pragma unroll
;       for (int e = 0; e < 4; ++e) { p0[4 * g + e] = a[e]; p1[4 * g + e] = c[e]; } }
; #pragma unroll
;     for (int ks = 0; ks < 4; ++ks) {
;       const bf16x8 k0 = *(const bf16x8*)(Ks + swz(r32, 2 * ks + hi)), k1 = *(const bf16x8*)(Ks + swz(32 + r32, 2 * ks + hi));
;       p0 = MFMA32(k0, qr[ks], p0); p1 = MFMA32(k1, qr[ks], p1);
;     }
;     if (j >= 2 * qb) {
;       const int kb = j * 64;
; #pragma unroll
;       for (int r = 0; r < 16; ++r) { const int kv = kb + crow(r, hi); if (kv > qrow) p0[r] = -INFINITY; if (kv + 32 > qrow) p1[r] = -INFINITY; }
;     ...
;         const int rowa = 32 * pb + 16 * s + 4 * hi + ((lane & 15) >> 2);
; #pragma unroll
;         for (int d0 = 0; d0 < 2; ++d0) {
;           const int cl = 4 * d0 + 2 * ((lane >> 4) & 1) + ((lane & 3) >> 1), sub = 8 * (lane & 1);
;           const s16x4 lo = tr16(Vs3 + swzv(rowa, cl) + sub), hi4 = tr16(Vs3 + swzv(rowa + 8, cl) + sub);
;           const bf16x8 vf = cat8(lo, hi4);
;           if (d0 == 0) o0 = MFMA32(vf, pf[pb][s], o0); else o1 = MFMA32(vf, pf[pb][s], o1);
.LBB0_1277:
	ds_read_b128 v[50:53], v128 offset:16384
	ds_read_b128 v[54:57], v128 offset:16416
	ds_read_b128 v[58:61], v128 offset:16448
	ds_read_b128 v[62:65], v128 offset:16480
	ds_read_b128 v[150:153], v136
	ds_read_b128 v[34:37], v128 offset:16512
	ds_read_b128 v[38:41], v128 offset:16544
	ds_read_b128 v[42:45], v128 offset:16576
	ds_read_b128 v[46:49], v128 offset:16608
	ds_read_b128 v[154:157], v136 offset:4096
	ds_read_b128 v[160:163], v137
	ds_read_b128 v[164:167], v137 offset:4096
	ds_read_b128 v[168:171], v138
	ds_read_b128 v[172:175], v138 offset:4096
	v_cmp_ge_i32_e64 s[8:9], v124, v105
	s_waitcnt lgkmcnt(9)
	v_mfma_f32_32x32x16_bf16 v[50:65], v[150:153], v[86:89], v[50:65]
	ds_read_b128 v[178:181], v139
	ds_read_b128 v[182:185], v139 offset:4096
	s_waitcnt lgkmcnt(6)
	v_mfma_f32_32x32x16_bf16 v[34:49], v[154:157], v[86:89], v[34:49]
	s_waitcnt lgkmcnt(5)
	v_mfma_f32_32x32x16_bf16 v[50:65], v[160:163], v[90:93], v[50:65]
	s_waitcnt lgkmcnt(4)
	v_mfma_f32_32x32x16_bf16 v[34:49], v[164:167], v[90:93], v[34:49]
	s_waitcnt lgkmcnt(3)
	v_mfma_f32_32x32x16_bf16 v[50:65], v[168:171], v[94:97], v[50:65]
	s_waitcnt lgkmcnt(2)
	v_mfma_f32_32x32x16_bf16 v[34:49], v[172:175], v[94:97], v[34:49]
	s_waitcnt lgkmcnt(1)
	v_mfma_f32_32x32x16_bf16 v[50:65], v[178:181], v[98:101], v[50:65]
	s_waitcnt lgkmcnt(0)
	v_mfma_f32_32x32x16_bf16 v[34:49], v[182:185], v[98:101], v[34:49]
	ds_read_b64_tr_b16 v[150:151], v140 offset:8192
	ds_read_b64_tr_b16 v[152:153], v141 offset:9216
	ds_read_b64_tr_b16 v[154:155], v142 offset:8192
	ds_read_b64_tr_b16 v[156:157], v143 offset:9216
	ds_read_b64_tr_b16 v[160:161], v140 offset:10240
	ds_read_b64_tr_b16 v[162:163], v141 offset:11264
	ds_read_b64_tr_b16 v[164:165], v142 offset:10240
	ds_read_b64_tr_b16 v[166:167], v143 offset:11264
	s_and_saveexec_b64 s[10:11], s[8:9]
	s_cbranch_execz .LBB0_1279
	v_or_b32_e32 v0, v149, v110
	v_or_b32_e32 v115, 32, v0
	v_cmp_le_i32_e64 s[8:9], v115, v104
	v_or_b32_e32 v115, 33, v0
	s_nop 5
	v_cndmask_b32_e64 v34, v119, v34, s[8:9]
	v_cmp_lt_i32_e64 s[8:9], v0, v104
	s_nop 1
	v_cndmask_b32_e64 v51, v119, v51, s[8:9]
	v_cmp_le_i32_e64 s[8:9], v0, v104
	s_nop 1
	v_cndmask_b32_e64 v50, v119, v50, s[8:9]
	v_cmp_le_i32_e64 s[8:9], v115, v104
	v_or_b32_e32 v115, 2, v0
	s_nop 0
	v_cndmask_b32_e64 v35, v119, v35, s[8:9]
	v_cmp_le_i32_e64 s[8:9], v115, v104
	v_or_b32_e32 v115, 34, v0
	s_nop 0
	v_cndmask_b32_e64 v52, v119, v52, s[8:9]
	v_cmp_le_i32_e64 s[8:9], v115, v104
	v_or_b32_e32 v115, 3, v0
	s_nop 0
	v_cndmask_b32_e64 v36, v119, v36, s[8:9]
	v_cmp_le_i32_e64 s[8:9], v115, v104
	v_or_b32_e32 v115, 35, v0
	s_nop 0
	v_cndmask_b32_e64 v53, v119, v53, s[8:9]
	v_cmp_le_i32_e64 s[8:9], v115, v104
	v_or_b32_e32 v115, 8, v0
	s_nop 0
	v_cndmask_b32_e64 v37, v119, v37, s[8:9]
	v_cmp_le_i32_e64 s[8:9], v115, v104
	v_or_b32_e32 v115, 40, v0
	s_nop 0
	v_cndmask_b32_e64 v54, v119, v54, s[8:9]
	v_cmp_le_i32_e64 s[8:9], v115, v104
	v_or_b32_e32 v115, 9, v0
	s_nop 0
	v_cndmask_b32_e64 v38, v119, v38, s[8:9]
	v_cmp_le_i32_e64 s[8:9], v115, v104
	v_or_b32_e32 v115, 41, v0
	s_nop 0
	v_cndmask_b32_e64 v55, v119, v55, s[8:9]
	v_cmp_le_i32_e64 s[8:9], v115, v104
	v_or_b32_e32 v115, 10, v0
	s_nop 0
	v_cndmask_b32_e64 v39, v119, v39, s[8:9]
	v_cmp_le_i32_e64 s[8:9], v115, v104
	v_or_b32_e32 v115, 42, v0
	s_nop 0
	v_cndmask_b32_e64 v56, v119, v56, s[8:9]
	v_cmp_le_i32_e64 s[8:9], v115, v104
	v_or_b32_e32 v115, 11, v0
	s_nop 0
	v_cndmask_b32_e64 v40, v119, v40, s[8:9]
	v_cmp_le_i32_e64 s[8:9], v115, v104
	v_or_b32_e32 v115, 43, v0
	s_nop 0
	v_cndmask_b32_e64 v57, v119, v57, s[8:9]
	v_cmp_le_i32_e64 s[8:9], v115, v104
	v_or_b32_e32 v115, 16, v0
	s_nop 0
	v_cndmask_b32_e64 v41, v119, v41, s[8:9]
	v_cmp_le_i32_e64 s[8:9], v115, v104
	v_or_b32_e32 v115, 48, v0
	s_nop 0
	v_cndmask_b32_e64 v58, v119, v58, s[8:9]
	v_cmp_le_i32_e64 s[8:9], v115, v104
	v_or_b32_e32 v115, 17, v0
	s_nop 0
	v_cndmask_b32_e64 v42, v119, v42, s[8:9]
	v_cmp_le_i32_e64 s[8:9], v115, v104
	v_or_b32_e32 v115, 49, v0
	s_nop 0
	v_cndmask_b32_e64 v59, v119, v59, s[8:9]
	v_cmp_le_i32_e64 s[8:9], v115, v104
	v_or_b32_e32 v115, 18, v0
	s_nop 0
	v_cndmask_b32_e64 v43, v119, v43, s[8:9]
	v_cmp_le_i32_e64 s[8:9], v115, v104
	v_or_b32_e32 v115, 50, v0
	s_nop 0
	v_cndmask_b32_e64 v60, v119, v60, s[8:9]
	v_cmp_le_i32_e64 s[8:9], v115, v104
	v_or_b32_e32 v115, 19, v0
	s_nop 0
	v_cndmask_b32_e64 v44, v119, v44, s[8:9]
	v_cmp_le_i32_e64 s[8:9], v115, v104
	v_or_b32_e32 v115, 51, v0
	s_nop 0
	v_cndmask_b32_e64 v61, v119, v61, s[8:9]
	v_cmp_le_i32_e64 s[8:9], v115, v104
	v_or_b32_e32 v115, 24, v0
	s_nop 0
	v_cndmask_b32_e64 v45, v119, v45, s[8:9]
	v_cmp_le_i32_e64 s[8:9], v115, v104
	v_or_b32_e32 v115, 56, v0
	s_nop 0
	v_cndmask_b32_e64 v62, v119, v62, s[8:9]
	v_cmp_le_i32_e64 s[8:9], v115, v104
	v_or_b32_e32 v115, 25, v0
	s_nop 0
	v_cndmask_b32_e64 v46, v119, v46, s[8:9]
	v_cmp_le_i32_e64 s[8:9], v115, v104
	v_or_b32_e32 v115, 57, v0
	s_nop 0
	v_cndmask_b32_e64 v63, v119, v63, s[8:9]
	v_cmp_le_i32_e64 s[8:9], v115, v104
	v_or_b32_e32 v115, 26, v0
	s_nop 0
	v_cndmask_b32_e64 v47, v119, v47, s[8:9]
	v_cmp_le_i32_e64 s[8:9], v115, v104
	v_or_b32_e32 v115, 58, v0
	s_nop 0
	v_cndmask_b32_e64 v64, v119, v64, s[8:9]
	v_cmp_le_i32_e64 s[8:9], v115, v104
	v_or_b32_e32 v115, 27, v0
	v_or_b32_e32 v0, 59, v0
	v_cndmask_b32_e64 v48, v119, v48, s[8:9]
	v_cmp_le_i32_e64 s[8:9], v115, v104
	s_nop 1
	v_cndmask_b32_e64 v65, v119, v65, s[8:9]
	v_cmp_le_i32_e64 s[8:9], v0, v104
	s_nop 1
	v_cndmask_b32_e64 v49, v119, v49, s[8:9]
; #define MFMA32(a, b, c) __builtin_amdgcn_mfma_f32_32x32x16_bf16((a), (b), (c), 0, 0, 0)
; DI s16x4 tr16(const LAS char* p) { typedef short v4i16_t __attribute__((ext_vector_type(4))); return __builtin_bit_cast(s16x4, __builtin_amdgcn_ds_read_tr16_b64_v4i16((LAS v4i16_t*)p)); }
; DI bf16x8 cat8(s16x4 lo, s16x4 hi) { return __builtin_shufflevector(lo, hi, 0, 1, 2, 3, 4, 5, 6, 7); }
; DI void attn_unit(const Params& p, int bh, int qb, char* lds, volatile LAS unsigned* hbc, unsigned& hbph) {
;     ...
;     float mx = fmaxf(p0[0], p1[0]);
; #pragma unroll
;     for (int r = 1; r < 16; ++r) mx = fmaxf(mx, fmaxf(p0[r], p1[r]));
;     mx = fmaxf(mx, __shfl_xor(mx, 32));
;     const float mn = fmaxf(m, mx), alpha = exp2f(m - mn); m = mn;
;     float ps = 0.f;
; #pragma unroll
;     for (int r = 0; r < 16; ++r) { p0[r] = exp2f(p0[r] - mn); p1[r] = exp2f(p1[r] - mn); ps += p0[r] + p1[r]; }
;     l = l * alpha + ps;
; #pragma unroll
;     for (int r = 0; r < 16; ++r) { o0[r] *= alpha; o1[r] *= alpha; }
;     bf16x8 pf[2][2];
;     pf[0][0] = pack8(p0[0], p0[1], p0[2], p0[3], p0[4], p0[5], p0[6], p0[7]);
;     pf[0][1] = pack8(p0[8], p0[9], p0[10], p0[11], p0[12], p0[13], p0[14], p0[15]);
;     pf[1][0] = pack8(p1[0], p1[1], p1[2], p1[3], p1[4], p1[5], p1[6], p1[7]);
;     pf[1][1] = pack8(p1[8], p1[9], p1[10], p1[11], p1[12], p1[13], p1[14], p1[15]);
; #pragma unroll
;     for (int pb = 0; pb < 2; ++pb)
; #pragma unroll
;       for (int s = 0; s < 2; ++s) {
;         const int rowa = 32 * pb + 16 * s + 4 * hi + ((lane & 15) >> 2);
; #pragma unroll
;         for (int d0 = 0; d0 < 2; ++d0) {
;           const int cl = 4 * d0 + 2 * ((lane >> 4) & 1) + ((lane & 3) >> 1), sub = 8 * (lane & 1);
;           const s16x4 lo = tr16(Vs3 + swzv(rowa, cl) + sub), hi4 = tr16(Vs3 + swzv(rowa + 8, cl) + sub);
;           const bf16x8 vf = cat8(lo, hi4);
;           if (d0 == 0) o0 = MFMA32(vf, pf[pb][s], o0); else o1 = MFMA32(vf, pf[pb][s], o1);
;         }
;       }
;     }
.LBB0_1279:
	s_or_b64 exec, exec, s[10:11]
	s_nop 8
	v_max3_f32 v0, v50, v51, v52
	v_max3_f32 v115, v53, v54, v55
	v_max3_f32 v159, v56, v57, v58
	v_max3_f32 v177, v59, v60, v61
	v_max3_f32 v186, v62, v63, v64
	v_max3_f32 v187, v65, v34, v35
	v_max3_f32 v168, v36, v37, v38
	v_max3_f32 v169, v39, v40, v41
	v_max3_f32 v170, v42, v43, v44
	v_max3_f32 v171, v45, v46, v47
	v_max3_f32 v0, v48, v49, v0
	v_max3_f32 v115, v115, v159, v177
	v_max3_f32 v186, v186, v187, v168
	v_max3_f32 v169, v169, v170, v171
	v_max3_f32 v0, v0, v115, v186
	v_max_f32_e32 v0, v0, v169
	v_mov_b32_e32 v168, v0
	v_mov_b32_e32 v169, v0
	s_nop 1
	v_permlane32_swap_b32_e32 v168, v169
	v_max3_f32 v0, v114, v168, v169
	v_sub_f32_e32 v172, v114, v0
	v_exp_f32_e32 v172, v172
	v_mov_b32_e32 v114, v0
	v_pk_add_f32 v[50:51], v[50:51], v[0:1] op_sel_hi:[1,0] neg_lo:[0,1] neg_hi:[0,1]
	v_pk_add_f32 v[52:53], v[52:53], v[0:1] op_sel_hi:[1,0] neg_lo:[0,1] neg_hi:[0,1]
	v_pk_add_f32 v[54:55], v[54:55], v[0:1] op_sel_hi:[1,0] neg_lo:[0,1] neg_hi:[0,1]
	v_pk_add_f32 v[56:57], v[56:57], v[0:1] op_sel_hi:[1,0] neg_lo:[0,1] neg_hi:[0,1]
	v_exp_f32_e32 v50, v50
	v_exp_f32_e32 v51, v51
	v_exp_f32_e32 v52, v52
	v_exp_f32_e32 v53, v53
	v_exp_f32_e32 v54, v54
	v_exp_f32_e32 v55, v55
	v_exp_f32_e32 v56, v56
	v_exp_f32_e32 v57, v57
	v_pk_mul_f32 v[18:19], v[18:19], v[172:173] op_sel_hi:[1,0]
	v_pk_mul_f32 v[20:21], v[20:21], v[172:173] op_sel_hi:[1,0]
	v_pk_mul_f32 v[22:23], v[22:23], v[172:173] op_sel_hi:[1,0]
	v_pk_mul_f32 v[24:25], v[24:25], v[172:173] op_sel_hi:[1,0]
	v_pk_mul_f32 v[26:27], v[26:27], v[172:173] op_sel_hi:[1,0]
	v_pk_mul_f32 v[28:29], v[28:29], v[172:173] op_sel_hi:[1,0]
	v_pk_mul_f32 v[30:31], v[30:31], v[172:173] op_sel_hi:[1,0]
	v_pk_mul_f32 v[32:33], v[32:33], v[172:173] op_sel_hi:[1,0]
	v_cvt_pk_bf16_f32 v168, v50, v51
	v_cvt_pk_bf16_f32 v169, v52, v53
	v_cvt_pk_bf16_f32 v170, v54, v55
	v_cvt_pk_bf16_f32 v171, v56, v57
	v_pk_add_f32 v[174:175], v[50:51], v[52:53]
	v_pk_add_f32 v[174:175], v[174:175], v[54:55]
	v_pk_add_f32 v[174:175], v[174:175], v[56:57]
	s_waitcnt lgkmcnt(0)
	v_mfma_f32_32x32x16_bf16 v[18:33], v[150:153], v[168:171], v[18:33]
	v_pk_mul_f32 v[2:3], v[2:3], v[172:173] op_sel_hi:[1,0]
	v_pk_mul_f32 v[4:5], v[4:5], v[172:173] op_sel_hi:[1,0]
	v_pk_mul_f32 v[6:7], v[6:7], v[172:173] op_sel_hi:[1,0]
	v_pk_mul_f32 v[8:9], v[8:9], v[172:173] op_sel_hi:[1,0]
	v_pk_mul_f32 v[10:11], v[10:11], v[172:173] op_sel_hi:[1,0]
	v_pk_mul_f32 v[12:13], v[12:13], v[172:173] op_sel_hi:[1,0]
	v_pk_mul_f32 v[14:15], v[14:15], v[172:173] op_sel_hi:[1,0]
	v_pk_mul_f32 v[16:17], v[16:17], v[172:173] op_sel_hi:[1,0]
	ds_read_b64_tr_b16 v[150:151], v140 offset:12288
	ds_read_b64_tr_b16 v[152:153], v141 offset:13312
	v_mfma_f32_32x32x16_bf16 v[2:17], v[154:157], v[168:171], v[2:17]
	ds_read_b64_tr_b16 v[154:155], v142 offset:12288
	ds_read_b64_tr_b16 v[156:157], v143 offset:13312
	v_pk_add_f32 v[58:59], v[58:59], v[0:1] op_sel_hi:[1,0] neg_lo:[0,1] neg_hi:[0,1]
	v_pk_add_f32 v[60:61], v[60:61], v[0:1] op_sel_hi:[1,0] neg_lo:[0,1] neg_hi:[0,1]
	v_pk_add_f32 v[62:63], v[62:63], v[0:1] op_sel_hi:[1,0] neg_lo:[0,1] neg_hi:[0,1]
	v_pk_add_f32 v[64:65], v[64:65], v[0:1] op_sel_hi:[1,0] neg_lo:[0,1] neg_hi:[0,1]
	v_exp_f32_e32 v58, v58
	v_exp_f32_e32 v59, v59
	v_exp_f32_e32 v60, v60
	v_exp_f32_e32 v61, v61
	v_exp_f32_e32 v62, v62
	v_exp_f32_e32 v63, v63
	v_exp_f32_e32 v64, v64
	v_exp_f32_e32 v65, v65
	v_cvt_pk_bf16_f32 v178, v58, v59
	v_cvt_pk_bf16_f32 v179, v60, v61
	v_cvt_pk_bf16_f32 v180, v62, v63
	v_cvt_pk_bf16_f32 v181, v64, v65
	v_pk_add_f32 v[174:175], v[174:175], v[58:59]
	v_pk_add_f32 v[174:175], v[174:175], v[60:61]
	v_pk_add_f32 v[174:175], v[174:175], v[62:63]
	v_pk_add_f32 v[174:175], v[174:175], v[64:65]
	v_mfma_f32_32x32x16_bf16 v[18:33], v[160:163], v[178:181], v[18:33]
	v_mfma_f32_32x32x16_bf16 v[2:17], v[164:167], v[178:181], v[2:17]
	ds_read_b64_tr_b16 v[160:161], v140 offset:14336
	ds_read_b64_tr_b16 v[162:163], v141 offset:15360
	ds_read_b64_tr_b16 v[164:165], v142 offset:14336
	ds_read_b64_tr_b16 v[166:167], v143 offset:15360
	v_pk_add_f32 v[34:35], v[34:35], v[0:1] op_sel_hi:[1,0] neg_lo:[0,1] neg_hi:[0,1]
	v_pk_add_f32 v[36:37], v[36:37], v[0:1] op_sel_hi:[1,0] neg_lo:[0,1] neg_hi:[0,1]
	v_pk_add_f32 v[38:39], v[38:39], v[0:1] op_sel_hi:[1,0] neg_lo:[0,1] neg_hi:[0,1]
	v_pk_add_f32 v[40:41], v[40:41], v[0:1] op_sel_hi:[1,0] neg_lo:[0,1] neg_hi:[0,1]
	v_exp_f32_e32 v34, v34
	v_exp_f32_e32 v35, v35
	v_exp_f32_e32 v36, v36
	v_exp_f32_e32 v37, v37
	v_exp_f32_e32 v38, v38
	v_exp_f32_e32 v39, v39
	v_exp_f32_e32 v40, v40
	v_exp_f32_e32 v41, v41
	v_cvt_pk_bf16_f32 v182, v34, v35
	v_cvt_pk_bf16_f32 v183, v36, v37
	v_cvt_pk_bf16_f32 v184, v38, v39
	v_cvt_pk_bf16_f32 v185, v40, v41
	v_pk_add_f32 v[174:175], v[174:175], v[34:35]
	v_pk_add_f32 v[174:175], v[174:175], v[36:37]
	v_pk_add_f32 v[174:175], v[174:175], v[38:39]
	v_pk_add_f32 v[174:175], v[174:175], v[40:41]
	s_waitcnt lgkmcnt(4)
	v_mfma_f32_32x32x16_bf16 v[18:33], v[150:153], v[182:185], v[18:33]
	v_mfma_f32_32x32x16_bf16 v[2:17], v[154:157], v[182:185], v[2:17]
	v_pk_add_f32 v[42:43], v[42:43], v[0:1] op_sel_hi:[1,0] neg_lo:[0,1] neg_hi:[0,1]
	v_pk_add_f32 v[44:45], v[44:45], v[0:1] op_sel_hi:[1,0] neg_lo:[0,1] neg_hi:[0,1]
	v_pk_add_f32 v[46:47], v[46:47], v[0:1] op_sel_hi:[1,0] neg_lo:[0,1] neg_hi:[0,1]
	v_pk_add_f32 v[48:49], v[48:49], v[0:1] op_sel_hi:[1,0] neg_lo:[0,1] neg_hi:[0,1]
	v_exp_f32_e32 v42, v42
	v_exp_f32_e32 v43, v43
	v_exp_f32_e32 v44, v44
	v_exp_f32_e32 v45, v45
	v_exp_f32_e32 v46, v46
	v_exp_f32_e32 v47, v47
	v_exp_f32_e32 v48, v48
	v_exp_f32_e32 v49, v49
	v_cvt_pk_bf16_f32 v190, v42, v43
	v_cvt_pk_bf16_f32 v191, v44, v45
	v_cvt_pk_bf16_f32 v192, v46, v47
	v_cvt_pk_bf16_f32 v193, v48, v49
	v_pk_add_f32 v[174:175], v[174:175], v[42:43]
	v_pk_add_f32 v[174:175], v[174:175], v[44:45]
	v_pk_add_f32 v[174:175], v[174:175], v[46:47]
	v_pk_add_f32 v[174:175], v[174:175], v[48:49]
	v_add_f32_e32 v174, v174, v175
	v_fma_f32 v133, v133, v172, v174
	s_waitcnt lgkmcnt(0)
	v_mfma_f32_32x32x16_bf16 v[18:33], v[160:163], v[190:193], v[18:33]
	v_mfma_f32_32x32x16_bf16 v[2:17], v[164:167], v[190:193], v[2:17]
	s_or_b64 exec, exec, s[38:39]
	v_and_b32_e32 v0, 4, v145
	s_and_saveexec_b64 s[10:11], s[34:35]
	s_cbranch_execz .LBB0_1252
